# v83 + block top-k loop: taken candidates marked, the four selection words built once after the loop instead of updated every iteration
# speedup vs baseline: 1.0038x; 1.0038x over previous
; #define DPP_I(x, ctrl) __builtin_amdgcn_update_dpp((int)(x), (int)(x), (ctrl), 0xF, 0xF, true)
; __device__ __forceinline__ void ph_attn_fast2(const Args& a, LAS unsigned char* lds) {
;     ...
;                     for (int it = 0; it < nsel - nforced; ++it) {
;                         int bv = max(max(max(vi[0], vi[1]), max(vi[2], vi[3])), max(max(vi[4], vi[5]), max(vi[6], vi[7])));
;                         bv = max(bv, DPP_I(bv, 0xB1)); bv = max(bv, DPP_I(bv, 0x4E)); bv = max(bv, DPP_I(bv, 0x141)); bv = max(bv, DPP_I(bv, 0x140));
;                         int bi = 255;
; #pragma unroll
;                         for (int k = 7; k >= 0; --k) bi = (vi[k] == bv) ? (li + 16 * k) : bi;
;                         bi = min(bi, DPP_I(bi, 0xB1)); bi = min(bi, DPP_I(bi, 0x4E)); bi = min(bi, DPP_I(bi, 0x141)); bi = min(bi, DPP_I(bi, 0x140));
;                         const unsigned bit = 1u << (bi & 31); const int wsel = bi >> 5;
;                         mm[0] |= (wsel == 0) ? bit : 0u; mm[1] |= (wsel == 1) ? bit : 0u; mm[2] |= (wsel == 2) ? bit : 0u; mm[3] |= (wsel == 3) ? bit : 0u;
;                         if ((bi & 15) == li) {
; #pragma unroll
;                             for (int k = 0; k < 8; ++k) if ((bi >> 4) == k) vi[k] = (int)0xFF800000;
;                         }
;                     }
;                     if (li == 0) { mskl[(4 * rnd + tl) * 4 + 0] = mm[0]; mskl[(4 * rnd + tl) * 4 + 1] = mm[1]; mskl[(4 * rnd + tl) * 4 + 2] = mm[2]; mskl[(4 * rnd + tl) * 4 + 3] = mm[3]; }
.LBB0_1999:
	s_or_b64 exec, exec, s[24:25]
	s_andn2_b64 vcc, exec, s[22:23]
	v_mov_b64_e32 v[4:5], s[16:17]
	v_mov_b32_e32 v13, s29
	v_mov_b32_e32 v10, s28
	s_cbranch_vccnz .LBB0_2004
	v_bfrev_b32_e32 v253, 1
	s_mov_b32 s26, 0
	v_mov_b32_e32 v13, s29
	v_mov_b32_e32 v10, s28
	v_mov_b64_e32 v[4:5], s[16:17]
	s_branch .LBB0_2002
.LBB0_2002:
	v_max3_i32 v19, v11, v2, v14
	v_max3_i32 v20, v12, v16, v15
	v_max3_i32 v19, v18, v17, v19
	v_max_i32_e32 v19, v19, v20
	s_nop 1
	v_max_i32_dpp v19, v19, v19 quad_perm:[1,0,3,2] row_mask:0xf bank_mask:0xf bound_ctrl:1
	s_nop 1
	v_max_i32_dpp v19, v19, v19 quad_perm:[2,3,0,1] row_mask:0xf bank_mask:0xf bound_ctrl:1
	s_nop 1
	v_max_i32_dpp v19, v19, v19 row_half_mirror row_mask:0xf bank_mask:0xf bound_ctrl:1
	s_nop 1
	v_max_i32_dpp v19, v19, v19 row_mirror row_mask:0xf bank_mask:0xf bound_ctrl:1
	v_cmp_eq_u32_e64 s[32:33], v17, v19
	v_cmp_eq_u32_e64 s[98:99], v18, v19
	v_cmp_eq_u32_e64 s[100:101], v15, v19
	v_cndmask_b32_e64 v20, v247, v240, s[32:33]
	v_cmp_eq_u32_e64 s[32:33], v16, v19
	v_cndmask_b32_e64 v20, v20, v238, s[98:99]
	v_cmp_eq_u32_e64 s[98:99], v12, v19
	v_cndmask_b32_e64 v20, v20, v236, s[100:101]
	v_cmp_eq_u32_e64 s[100:101], v14, v19
	v_cndmask_b32_e64 v20, v20, v234, s[32:33]
	v_cmp_eq_u32_e64 s[32:33], v2, v19
	v_cndmask_b32_e64 v20, v20, v232, s[98:99]
	v_cmp_eq_u32_e64 s[98:99], v11, v19
	v_cndmask_b32_e64 v20, v20, v230, s[100:101]
	v_cndmask_b32_e64 v20, v20, v228, s[32:33]
	v_cndmask_b32_e64 v19, v20, v211, s[98:99]
	s_nop 1
	v_min_i32_dpp v19, v19, v19 quad_perm:[1,0,3,2] row_mask:0xf bank_mask:0xf bound_ctrl:1
	s_nop 1
	v_min_i32_dpp v19, v19, v19 quad_perm:[2,3,0,1] row_mask:0xf bank_mask:0xf bound_ctrl:1
	s_nop 1
	v_min_i32_dpp v19, v19, v19 row_half_mirror row_mask:0xf bank_mask:0xf bound_ctrl:1
	s_nop 1
	v_min_i32_dpp v19, v19, v19 row_mirror row_mask:0xf bank_mask:0xf bound_ctrl:1
	v_cmp_eq_u32_e64 s[32:33], v19, v211
	v_cmp_eq_u32_e64 s[98:99], v19, v228
	v_cmp_eq_u32_e64 s[100:101], v19, v230
	v_cndmask_b32_e64 v11, v11, v253, s[32:33]
	v_cmp_eq_u32_e64 s[32:33], v19, v232
	v_cndmask_b32_e64 v2, v2, v253, s[98:99]
	v_cmp_eq_u32_e64 s[98:99], v19, v234
	v_cndmask_b32_e64 v14, v14, v253, s[100:101]
	v_cmp_eq_u32_e64 s[100:101], v19, v236
	v_cndmask_b32_e64 v12, v12, v253, s[32:33]
	v_cmp_eq_u32_e64 s[32:33], v19, v238
	v_cndmask_b32_e64 v16, v16, v253, s[98:99]
	v_cmp_eq_u32_e64 s[98:99], v19, v240
	v_cndmask_b32_e64 v15, v15, v253, s[100:101]
	v_cndmask_b32_e64 v18, v18, v253, s[32:33]
	v_cndmask_b32_e64 v17, v17, v253, s[98:99]
	s_add_i32 s26, s26, 1
	s_cmp_ge_i32 s26, s30
	s_cbranch_scc0 .LBB0_2002
	v_lshlrev_b32_e64 v20, v211, 1
	v_lshlrev_b32_e32 v21, 16, v20
	v_cmp_eq_u32_e64 s[32:33], v11, v253
	v_cmp_eq_u32_e64 s[98:99], v2, v253
	v_cmp_eq_u32_e64 s[100:101], v14, v253
	v_cndmask_b32_e64 v11, 0, v20, s[32:33]
	v_cmp_eq_u32_e64 s[32:33], v12, v253
	v_cndmask_b32_e64 v2, 0, v21, s[98:99]
	v_cmp_eq_u32_e64 s[98:99], v16, v253
	v_cndmask_b32_e64 v14, 0, v20, s[100:101]
	v_cmp_eq_u32_e64 s[100:101], v15, v253
	v_cndmask_b32_e64 v12, 0, v21, s[32:33]
	v_cmp_eq_u32_e64 s[32:33], v18, v253
	v_cndmask_b32_e64 v16, 0, v20, s[98:99]
	v_cmp_eq_u32_e64 s[98:99], v17, v253
	v_cndmask_b32_e64 v15, 0, v21, s[100:101]
	v_cndmask_b32_e64 v18, 0, v20, s[32:33]
	v_cndmask_b32_e64 v17, 0, v21, s[98:99]
	v_or_b32_e32 v11, v11, v2
	v_or_b32_e32 v14, v14, v12
	v_or_b32_e32 v16, v16, v15
	v_or_b32_e32 v18, v18, v17
	v_or_b32_dpp v11, v11, v11 quad_perm:[1,0,3,2] row_mask:0xf bank_mask:0xf bound_ctrl:1
	v_or_b32_dpp v14, v14, v14 quad_perm:[1,0,3,2] row_mask:0xf bank_mask:0xf bound_ctrl:1
	v_or_b32_dpp v16, v16, v16 quad_perm:[1,0,3,2] row_mask:0xf bank_mask:0xf bound_ctrl:1
	v_or_b32_dpp v18, v18, v18 quad_perm:[1,0,3,2] row_mask:0xf bank_mask:0xf bound_ctrl:1
	v_or_b32_dpp v11, v11, v11 quad_perm:[2,3,0,1] row_mask:0xf bank_mask:0xf bound_ctrl:1
	v_or_b32_dpp v14, v14, v14 quad_perm:[2,3,0,1] row_mask:0xf bank_mask:0xf bound_ctrl:1
	v_or_b32_dpp v16, v16, v16 quad_perm:[2,3,0,1] row_mask:0xf bank_mask:0xf bound_ctrl:1
	v_or_b32_dpp v18, v18, v18 quad_perm:[2,3,0,1] row_mask:0xf bank_mask:0xf bound_ctrl:1
	v_or_b32_dpp v11, v11, v11 row_half_mirror row_mask:0xf bank_mask:0xf bound_ctrl:1
	v_or_b32_dpp v14, v14, v14 row_half_mirror row_mask:0xf bank_mask:0xf bound_ctrl:1
	v_or_b32_dpp v16, v16, v16 row_half_mirror row_mask:0xf bank_mask:0xf bound_ctrl:1
	v_or_b32_dpp v18, v18, v18 row_half_mirror row_mask:0xf bank_mask:0xf bound_ctrl:1
	v_or_b32_dpp v11, v11, v11 row_mirror row_mask:0xf bank_mask:0xf bound_ctrl:1
	v_or_b32_dpp v14, v14, v14 row_mirror row_mask:0xf bank_mask:0xf bound_ctrl:1
	v_or_b32_dpp v16, v16, v16 row_mirror row_mask:0xf bank_mask:0xf bound_ctrl:1
	v_or_b32_dpp v18, v18, v18 row_mirror row_mask:0xf bank_mask:0xf bound_ctrl:1
	v_or_b32_e32 v10, v10, v11
	v_or_b32_e32 v4, v4, v14
	v_or_b32_e32 v5, v5, v16
	v_or_b32_e32 v13, v13, v18
